# speedup vs baseline: 1.0260x; 1.0049x over previous
.LBB0_3:
	s_mov_b32 s4, 0xa000
	v_cmp_gt_u32_e32 vcc, s4, v2
	s_and_saveexec_b64 s[4:5], vcc
	s_cbranch_execz .LBB0_5
	s_load_dwordx2 s[6:7], s[0:1], 0x18
	s_load_dwordx2 s[8:9], s[0:1], 0x28
	v_add_u32_e32 v8, 0xffffa000, v2
	v_lshrrev_b32_e32 v1, 5, v8
	v_and_b32_e32 v3, 31, v0
	s_mov_b32 s10, 0xffffe0
	v_and_or_b32 v1, v1, s10, v3
	v_lshlrev_b32_e32 v10, 8, v1
	v_mov_b32_e32 v11, 0
	s_waitcnt lgkmcnt(0)
	v_lshl_add_u64 v[4:5], v[10:11], 2, s[6:7]
	v_and_b32_e32 v10, 0x380, v2
	v_lshl_add_u64 v[4:5], v[4:5], 0, v[10:11]
	v_and_b32_e32 v10, 64, v2
	v_lshrrev_b32_e32 v0, 1, v0
	v_lshl_add_u64 v[2:3], v[4:5], 0, v[10:11]
	v_and_b32_e32 v10, 16, v0
	v_lshl_add_u64 v[12:13], v[2:3], 0, v[10:11]
	global_load_dwordx4 v[0:3], v[12:13], off
	global_load_dwordx4 v[4:7], v[12:13], off offset:32
	v_mov_b32_e32 v9, v11
	s_waitcnt vmcnt(1)
	v_cvt_pk_f16_f32 v0, v0, v1
	v_cvt_pk_f16_f32 v1, v2, v3
	s_waitcnt vmcnt(0)
	v_cvt_pk_f16_f32 v2, v4, v5
	v_cvt_pk_f16_f32 v3, v6, v7
	v_lshl_add_u64 v[4:5], v[8:9], 4, s[8:9]
	global_store_dwordx4 v[4:5], v[0:3], off sc1

.LBB0_14:
	s_or_b64 exec, exec, s[4:5]
	v_lshrrev_b32_e32 v0, 2, v0
	v_lshrrev_b32_e32 v1, 2, v2
	v_and_b32_e32 v0, 8, v0
	s_movk_i32 s0, 0x1f0
	v_and_or_b32 v0, v1, s0, v0
	v_lshlrev_b32_e32 v0, 2, v0
	v_mov_b32_e32 v1, 0
	v_lshl_add_u64 v[0:1], v[4:5], 0, v[0:1]
	global_load_dwordx4 v[4:7], v[0:1], off
	global_load_dwordx4 v[8:11], v[0:1], off offset:16
	v_ashrrev_i32_e32 v3, 31, v2
	s_waitcnt lgkmcnt(0)
	v_lshl_add_u64 v[0:1], v[2:3], 4, s[2:3]
	s_waitcnt vmcnt(1)
	v_cvt_pk_f16_f32 v4, v4, v5
	v_cvt_pk_f16_f32 v5, v6, v7
	s_waitcnt vmcnt(0)
	v_cvt_pk_f16_f32 v6, v8, v9
	v_cvt_pk_f16_f32 v7, v10, v11
	global_store_dwordx4 v[0:1], v[4:7], off sc1
	s_endpgm

.Lk2_older:
	s_waitcnt vmcnt(12)
	v_mfma_f32_32x32x16_f16 v[96:111], v[32:35], v[0:3], 0
	v_mfma_f32_32x32x16_f16 v[112:127], v[32:35], v[16:19], 0
	v_mfma_f32_32x32x16_f16 v[96:111], v[36:39], v[4:7], v[96:111]
	v_mfma_f32_32x32x16_f16 v[112:127], v[36:39], v[20:23], v[112:127]
	v_mfma_f32_32x32x16_f16 v[96:111], v[40:43], v[8:11], v[96:111]
	v_mfma_f32_32x32x16_f16 v[112:127], v[40:43], v[24:27], v[112:127]
	v_mfma_f32_32x32x16_f16 v[96:111], v[44:47], v[12:15], v[96:111]
	v_mfma_f32_32x32x16_f16 v[112:127], v[44:47], v[28:31], v[112:127]
	global_load_dwordx4 v[32:35], v171, s[4:5] offset:0
	global_load_dwordx4 v[36:39], v171, s[4:5] offset:1024
	global_load_dwordx4 v[40:43], v171, s[4:5] offset:2048
	global_load_dwordx4 v[44:47], v171, s[4:5] offset:3072
	s_add_u32 s4, s4, 0x1000
	s_addc_u32 s5, s5, 0
	s_nop 7
	s_nop 3
	s_waitcnt vmcnt(12)
	v_mfma_f32_32x32x16_f16 v[128:143], v[48:51], v[0:3], 0
	v_exp_f32_e32 v96, v96
	v_exp_f32_e32 v97, v97
	v_exp_f32_e32 v98, v98
	v_exp_f32_e32 v99, v99
	v_mfma_f32_32x32x16_f16 v[144:159], v[48:51], v[16:19], 0
	v_exp_f32_e32 v100, v100
	v_exp_f32_e32 v101, v101
	v_exp_f32_e32 v102, v102
	v_exp_f32_e32 v103, v103
	v_pk_add_f32 v[160:161], v[160:161], v[96:97]
	v_pk_add_f32 v[162:163], v[162:163], v[98:99]
	v_mfma_f32_32x32x16_f16 v[128:143], v[52:55], v[4:7], v[128:143]
	v_exp_f32_e32 v104, v104
	v_exp_f32_e32 v105, v105
	v_exp_f32_e32 v106, v106
	v_exp_f32_e32 v107, v107
	v_pk_add_f32 v[160:161], v[160:161], v[100:101]
	v_pk_add_f32 v[162:163], v[162:163], v[102:103]
	v_mfma_f32_32x32x16_f16 v[144:159], v[52:55], v[20:23], v[144:159]
	v_exp_f32_e32 v108, v108
	v_exp_f32_e32 v109, v109
	v_exp_f32_e32 v110, v110
	v_exp_f32_e32 v111, v111
	v_pk_add_f32 v[160:161], v[160:161], v[104:105]
	v_pk_add_f32 v[162:163], v[162:163], v[106:107]
	v_mfma_f32_32x32x16_f16 v[128:143], v[56:59], v[8:11], v[128:143]
	v_exp_f32_e32 v112, v112
	v_exp_f32_e32 v113, v113
	v_exp_f32_e32 v114, v114
	v_exp_f32_e32 v115, v115
	v_pk_add_f32 v[160:161], v[160:161], v[108:109]
	v_pk_add_f32 v[162:163], v[162:163], v[110:111]
	v_mfma_f32_32x32x16_f16 v[144:159], v[56:59], v[24:27], v[144:159]
	v_exp_f32_e32 v116, v116
	v_exp_f32_e32 v117, v117
	v_exp_f32_e32 v118, v118
	v_exp_f32_e32 v119, v119
	v_pk_add_f32 v[164:165], v[164:165], v[112:113]
	v_pk_add_f32 v[166:167], v[166:167], v[114:115]
	v_mfma_f32_32x32x16_f16 v[128:143], v[60:63], v[12:15], v[128:143]
	v_exp_f32_e32 v120, v120
	v_exp_f32_e32 v121, v121
	v_exp_f32_e32 v122, v122
	v_exp_f32_e32 v123, v123
	v_pk_add_f32 v[164:165], v[164:165], v[116:117]
	v_pk_add_f32 v[166:167], v[166:167], v[118:119]
	v_mfma_f32_32x32x16_f16 v[144:159], v[60:63], v[28:31], v[144:159]
	v_exp_f32_e32 v124, v124
	v_exp_f32_e32 v125, v125
	v_exp_f32_e32 v126, v126
	v_exp_f32_e32 v127, v127
	v_pk_add_f32 v[164:165], v[164:165], v[120:121]
	v_pk_add_f32 v[166:167], v[166:167], v[122:123]
	s_nop 0
	v_pk_add_f32 v[164:165], v[164:165], v[124:125]
	v_pk_add_f32 v[166:167], v[166:167], v[126:127]
	global_load_dwordx4 v[48:51], v171, s[4:5] offset:0
	global_load_dwordx4 v[52:55], v171, s[4:5] offset:1024
	global_load_dwordx4 v[56:59], v171, s[4:5] offset:2048
	global_load_dwordx4 v[60:63], v171, s[4:5] offset:3072
	s_add_u32 s4, s4, 0x1000
	s_addc_u32 s5, s5, 0
	s_waitcnt vmcnt(12)
	v_mfma_f32_32x32x16_f16 v[96:111], v[64:67], v[0:3], 0
	v_exp_f32_e32 v128, v128
	v_exp_f32_e32 v129, v129
	v_exp_f32_e32 v130, v130
	v_exp_f32_e32 v131, v131
	v_mfma_f32_32x32x16_f16 v[112:127], v[64:67], v[16:19], 0
	v_exp_f32_e32 v132, v132
	v_exp_f32_e32 v133, v133
	v_exp_f32_e32 v134, v134
	v_exp_f32_e32 v135, v135
	v_pk_add_f32 v[160:161], v[160:161], v[128:129]
	v_pk_add_f32 v[162:163], v[162:163], v[130:131]
	v_mfma_f32_32x32x16_f16 v[96:111], v[68:71], v[4:7], v[96:111]
	v_exp_f32_e32 v136, v136
	v_exp_f32_e32 v137, v137
	v_exp_f32_e32 v138, v138
	v_exp_f32_e32 v139, v139
	v_pk_add_f32 v[160:161], v[160:161], v[132:133]
	v_pk_add_f32 v[162:163], v[162:163], v[134:135]
	v_mfma_f32_32x32x16_f16 v[112:127], v[68:71], v[20:23], v[112:127]
	v_exp_f32_e32 v140, v140
	v_exp_f32_e32 v141, v141
	v_exp_f32_e32 v142, v142
	v_exp_f32_e32 v143, v143
	v_pk_add_f32 v[160:161], v[160:161], v[136:137]
	v_pk_add_f32 v[162:163], v[162:163], v[138:139]
	v_mfma_f32_32x32x16_f16 v[96:111], v[72:75], v[8:11], v[96:111]
	v_exp_f32_e32 v144, v144
	v_exp_f32_e32 v145, v145
	v_exp_f32_e32 v146, v146
	v_exp_f32_e32 v147, v147
	v_pk_add_f32 v[160:161], v[160:161], v[140:141]
	v_pk_add_f32 v[162:163], v[162:163], v[142:143]
	v_mfma_f32_32x32x16_f16 v[112:127], v[72:75], v[24:27], v[112:127]
	v_exp_f32_e32 v148, v148
	v_exp_f32_e32 v149, v149
	v_exp_f32_e32 v150, v150
	v_exp_f32_e32 v151, v151
	v_pk_add_f32 v[164:165], v[164:165], v[144:145]
	v_pk_add_f32 v[166:167], v[166:167], v[146:147]
	v_mfma_f32_32x32x16_f16 v[96:111], v[76:79], v[12:15], v[96:111]
	v_exp_f32_e32 v152, v152
	v_exp_f32_e32 v153, v153
	v_exp_f32_e32 v154, v154
	v_exp_f32_e32 v155, v155
	v_pk_add_f32 v[164:165], v[164:165], v[148:149]
	v_pk_add_f32 v[166:167], v[166:167], v[150:151]
	v_mfma_f32_32x32x16_f16 v[112:127], v[76:79], v[28:31], v[112:127]
	v_exp_f32_e32 v156, v156
	v_exp_f32_e32 v157, v157
	v_exp_f32_e32 v158, v158
	v_exp_f32_e32 v159, v159
	v_pk_add_f32 v[164:165], v[164:165], v[152:153]
	v_pk_add_f32 v[166:167], v[166:167], v[154:155]
	s_nop 0
	v_pk_add_f32 v[164:165], v[164:165], v[156:157]
	v_pk_add_f32 v[166:167], v[166:167], v[158:159]
	global_load_dwordx4 v[64:67], v171, s[4:5] offset:0
	global_load_dwordx4 v[68:71], v171, s[4:5] offset:1024
	global_load_dwordx4 v[72:75], v171, s[4:5] offset:2048
	global_load_dwordx4 v[76:79], v171, s[4:5] offset:3072
	s_add_u32 s4, s4, 0x1000
	s_addc_u32 s5, s5, 0
	s_waitcnt vmcnt(12)
	v_mfma_f32_32x32x16_f16 v[128:143], v[80:83], v[0:3], 0
	v_exp_f32_e32 v96, v96
	v_exp_f32_e32 v97, v97
	v_exp_f32_e32 v98, v98
	v_exp_f32_e32 v99, v99
	v_mfma_f32_32x32x16_f16 v[144:159], v[80:83], v[16:19], 0
	v_exp_f32_e32 v100, v100
	v_exp_f32_e32 v101, v101
	v_exp_f32_e32 v102, v102
	v_exp_f32_e32 v103, v103
	v_pk_add_f32 v[160:161], v[160:161], v[96:97]
	v_pk_add_f32 v[162:163], v[162:163], v[98:99]
	v_mfma_f32_32x32x16_f16 v[128:143], v[84:87], v[4:7], v[128:143]
	v_exp_f32_e32 v104, v104
	v_exp_f32_e32 v105, v105
	v_exp_f32_e32 v106, v106
	v_exp_f32_e32 v107, v107
	v_pk_add_f32 v[160:161], v[160:161], v[100:101]
	v_pk_add_f32 v[162:163], v[162:163], v[102:103]
	v_mfma_f32_32x32x16_f16 v[144:159], v[84:87], v[20:23], v[144:159]
	v_exp_f32_e32 v108, v108
	v_exp_f32_e32 v109, v109
	v_exp_f32_e32 v110, v110
	v_exp_f32_e32 v111, v111
	v_pk_add_f32 v[160:161], v[160:161], v[104:105]
	v_pk_add_f32 v[162:163], v[162:163], v[106:107]
	v_mfma_f32_32x32x16_f16 v[128:143], v[88:91], v[8:11], v[128:143]
	v_exp_f32_e32 v112, v112
	v_exp_f32_e32 v113, v113
	v_exp_f32_e32 v114, v114
	v_exp_f32_e32 v115, v115
	v_pk_add_f32 v[160:161], v[160:161], v[108:109]
	v_pk_add_f32 v[162:163], v[162:163], v[110:111]
	v_mfma_f32_32x32x16_f16 v[144:159], v[88:91], v[24:27], v[144:159]
	v_exp_f32_e32 v116, v116
	v_exp_f32_e32 v117, v117
	v_exp_f32_e32 v118, v118
	v_exp_f32_e32 v119, v119
	v_pk_add_f32 v[164:165], v[164:165], v[112:113]
	v_pk_add_f32 v[166:167], v[166:167], v[114:115]
	v_mfma_f32_32x32x16_f16 v[128:143], v[92:95], v[12:15], v[128:143]
	v_exp_f32_e32 v120, v120
	v_exp_f32_e32 v121, v121
	v_exp_f32_e32 v122, v122
	v_exp_f32_e32 v123, v123
	v_pk_add_f32 v[164:165], v[164:165], v[116:117]
	v_pk_add_f32 v[166:167], v[166:167], v[118:119]
	v_mfma_f32_32x32x16_f16 v[144:159], v[92:95], v[28:31], v[144:159]
	v_exp_f32_e32 v124, v124
	v_exp_f32_e32 v125, v125
	v_exp_f32_e32 v126, v126
	v_exp_f32_e32 v127, v127
	v_pk_add_f32 v[164:165], v[164:165], v[120:121]
	v_pk_add_f32 v[166:167], v[166:167], v[122:123]
	s_nop 0
	v_pk_add_f32 v[164:165], v[164:165], v[124:125]
	v_pk_add_f32 v[166:167], v[166:167], v[126:127]
	global_load_dwordx4 v[80:83], v171, s[4:5] offset:0
	global_load_dwordx4 v[84:87], v171, s[4:5] offset:1024
	global_load_dwordx4 v[88:91], v171, s[4:5] offset:2048
	global_load_dwordx4 v[92:95], v171, s[4:5] offset:3072
	s_add_u32 s4, s4, 0x1000
	s_addc_u32 s5, s5, 0
	s_waitcnt vmcnt(12)
	v_mfma_f32_32x32x16_f16 v[96:111], v[32:35], v[0:3], 0
	v_exp_f32_e32 v128, v128
	v_exp_f32_e32 v129, v129
	v_exp_f32_e32 v130, v130
	v_exp_f32_e32 v131, v131
	v_mfma_f32_32x32x16_f16 v[112:127], v[32:35], v[16:19], 0
	v_exp_f32_e32 v132, v132
	v_exp_f32_e32 v133, v133
	v_exp_f32_e32 v134, v134
	v_exp_f32_e32 v135, v135
	v_pk_add_f32 v[160:161], v[160:161], v[128:129]
	v_pk_add_f32 v[162:163], v[162:163], v[130:131]
	v_mfma_f32_32x32x16_f16 v[96:111], v[36:39], v[4:7], v[96:111]
	v_exp_f32_e32 v136, v136
	v_exp_f32_e32 v137, v137
	v_exp_f32_e32 v138, v138
	v_exp_f32_e32 v139, v139
	v_pk_add_f32 v[160:161], v[160:161], v[132:133]
	v_pk_add_f32 v[162:163], v[162:163], v[134:135]
	v_mfma_f32_32x32x16_f16 v[112:127], v[36:39], v[20:23], v[112:127]
	v_exp_f32_e32 v140, v140
	v_exp_f32_e32 v141, v141
	v_exp_f32_e32 v142, v142
	v_exp_f32_e32 v143, v143
	v_pk_add_f32 v[160:161], v[160:161], v[136:137]
	v_pk_add_f32 v[162:163], v[162:163], v[138:139]
	v_mfma_f32_32x32x16_f16 v[96:111], v[40:43], v[8:11], v[96:111]
	v_exp_f32_e32 v144, v144
	v_exp_f32_e32 v145, v145
	v_exp_f32_e32 v146, v146
	v_exp_f32_e32 v147, v147
	v_pk_add_f32 v[160:161], v[160:161], v[140:141]
	v_pk_add_f32 v[162:163], v[162:163], v[142:143]
	v_mfma_f32_32x32x16_f16 v[112:127], v[40:43], v[24:27], v[112:127]
	v_exp_f32_e32 v148, v148
	v_exp_f32_e32 v149, v149
	v_exp_f32_e32 v150, v150
	v_exp_f32_e32 v151, v151
	v_pk_add_f32 v[164:165], v[164:165], v[144:145]
	v_pk_add_f32 v[166:167], v[166:167], v[146:147]
	v_mfma_f32_32x32x16_f16 v[96:111], v[44:47], v[12:15], v[96:111]
	v_exp_f32_e32 v152, v152
	v_exp_f32_e32 v153, v153
	v_exp_f32_e32 v154, v154
	v_exp_f32_e32 v155, v155
	v_pk_add_f32 v[164:165], v[164:165], v[148:149]
	v_pk_add_f32 v[166:167], v[166:167], v[150:151]
	v_mfma_f32_32x32x16_f16 v[112:127], v[44:47], v[28:31], v[112:127]
	v_exp_f32_e32 v156, v156
	v_exp_f32_e32 v157, v157
	v_exp_f32_e32 v158, v158
	v_exp_f32_e32 v159, v159
	v_pk_add_f32 v[164:165], v[164:165], v[152:153]
	v_pk_add_f32 v[166:167], v[166:167], v[154:155]
	s_nop 0
	v_pk_add_f32 v[164:165], v[164:165], v[156:157]
	v_pk_add_f32 v[166:167], v[166:167], v[158:159]
	global_load_dwordx4 v[32:35], v171, s[4:5] offset:0
	global_load_dwordx4 v[36:39], v171, s[4:5] offset:1024
	global_load_dwordx4 v[40:43], v171, s[4:5] offset:2048
	global_load_dwordx4 v[44:47], v171, s[4:5] offset:3072
	s_add_u32 s4, s4, 0x1000
	s_addc_u32 s5, s5, 0
	s_waitcnt vmcnt(12)
	v_mfma_f32_32x32x16_f16 v[128:143], v[48:51], v[0:3], 0
	v_exp_f32_e32 v96, v96
	v_exp_f32_e32 v97, v97
	v_exp_f32_e32 v98, v98
	v_exp_f32_e32 v99, v99
	v_mfma_f32_32x32x16_f16 v[144:159], v[48:51], v[16:19], 0
	v_exp_f32_e32 v100, v100
	v_exp_f32_e32 v101, v101
	v_exp_f32_e32 v102, v102
	v_exp_f32_e32 v103, v103
	v_pk_add_f32 v[160:161], v[160:161], v[96:97]
	v_pk_add_f32 v[162:163], v[162:163], v[98:99]
	v_mfma_f32_32x32x16_f16 v[128:143], v[52:55], v[4:7], v[128:143]
	v_exp_f32_e32 v104, v104
	v_exp_f32_e32 v105, v105
	v_exp_f32_e32 v106, v106
	v_exp_f32_e32 v107, v107
	v_pk_add_f32 v[160:161], v[160:161], v[100:101]
	v_pk_add_f32 v[162:163], v[162:163], v[102:103]
	v_mfma_f32_32x32x16_f16 v[144:159], v[52:55], v[20:23], v[144:159]
	v_exp_f32_e32 v108, v108
	v_exp_f32_e32 v109, v109
	v_exp_f32_e32 v110, v110
	v_exp_f32_e32 v111, v111
	v_pk_add_f32 v[160:161], v[160:161], v[104:105]
	v_pk_add_f32 v[162:163], v[162:163], v[106:107]
	v_mfma_f32_32x32x16_f16 v[128:143], v[56:59], v[8:11], v[128:143]
	v_exp_f32_e32 v112, v112
	v_exp_f32_e32 v113, v113
	v_exp_f32_e32 v114, v114
	v_exp_f32_e32 v115, v115
	v_pk_add_f32 v[160:161], v[160:161], v[108:109]
	v_pk_add_f32 v[162:163], v[162:163], v[110:111]
	v_mfma_f32_32x32x16_f16 v[144:159], v[56:59], v[24:27], v[144:159]
	v_exp_f32_e32 v116, v116
	v_exp_f32_e32 v117, v117
	v_exp_f32_e32 v118, v118
	v_exp_f32_e32 v119, v119
	v_pk_add_f32 v[164:165], v[164:165], v[112:113]
	v_pk_add_f32 v[166:167], v[166:167], v[114:115]
	v_mfma_f32_32x32x16_f16 v[128:143], v[60:63], v[12:15], v[128:143]
	v_exp_f32_e32 v120, v120
	v_exp_f32_e32 v121, v121
	v_exp_f32_e32 v122, v122
	v_exp_f32_e32 v123, v123
	v_pk_add_f32 v[164:165], v[164:165], v[116:117]
	v_pk_add_f32 v[166:167], v[166:167], v[118:119]
	v_mfma_f32_32x32x16_f16 v[144:159], v[60:63], v[28:31], v[144:159]
	v_exp_f32_e32 v124, v124
	v_exp_f32_e32 v125, v125
	v_exp_f32_e32 v126, v126
	v_exp_f32_e32 v127, v127
	v_pk_add_f32 v[164:165], v[164:165], v[120:121]
	v_pk_add_f32 v[166:167], v[166:167], v[122:123]
	s_nop 0
	v_pk_add_f32 v[164:165], v[164:165], v[124:125]
	v_pk_add_f32 v[166:167], v[166:167], v[126:127]
	global_load_dwordx4 v[48:51], v171, s[4:5] offset:0
	global_load_dwordx4 v[52:55], v171, s[4:5] offset:1024
	global_load_dwordx4 v[56:59], v171, s[4:5] offset:2048
	global_load_dwordx4 v[60:63], v171, s[4:5] offset:3072
	s_add_u32 s4, s4, 0x1000
	s_addc_u32 s5, s5, 0
	s_waitcnt vmcnt(12)
	v_mfma_f32_32x32x16_f16 v[96:111], v[64:67], v[0:3], 0
	v_exp_f32_e32 v128, v128
	v_exp_f32_e32 v129, v129
	v_exp_f32_e32 v130, v130
	v_exp_f32_e32 v131, v131
	v_mfma_f32_32x32x16_f16 v[112:127], v[64:67], v[16:19], 0
	v_exp_f32_e32 v132, v132
	v_exp_f32_e32 v133, v133
	v_exp_f32_e32 v134, v134
	v_exp_f32_e32 v135, v135
	v_pk_add_f32 v[160:161], v[160:161], v[128:129]
	v_pk_add_f32 v[162:163], v[162:163], v[130:131]
	v_mfma_f32_32x32x16_f16 v[96:111], v[68:71], v[4:7], v[96:111]
	v_exp_f32_e32 v136, v136
	v_exp_f32_e32 v137, v137
	v_exp_f32_e32 v138, v138
	v_exp_f32_e32 v139, v139
	v_pk_add_f32 v[160:161], v[160:161], v[132:133]
	v_pk_add_f32 v[162:163], v[162:163], v[134:135]
	v_mfma_f32_32x32x16_f16 v[112:127], v[68:71], v[20:23], v[112:127]
	v_exp_f32_e32 v140, v140
	v_exp_f32_e32 v141, v141
	v_exp_f32_e32 v142, v142
	v_exp_f32_e32 v143, v143
	v_pk_add_f32 v[160:161], v[160:161], v[136:137]
	v_pk_add_f32 v[162:163], v[162:163], v[138:139]
	v_mfma_f32_32x32x16_f16 v[96:111], v[72:75], v[8:11], v[96:111]
	v_exp_f32_e32 v144, v144
	v_exp_f32_e32 v145, v145
	v_exp_f32_e32 v146, v146
	v_exp_f32_e32 v147, v147
	v_pk_add_f32 v[160:161], v[160:161], v[140:141]
	v_pk_add_f32 v[162:163], v[162:163], v[142:143]
	v_mfma_f32_32x32x16_f16 v[112:127], v[72:75], v[24:27], v[112:127]
	v_exp_f32_e32 v148, v148
	v_exp_f32_e32 v149, v149
	v_exp_f32_e32 v150, v150
	v_exp_f32_e32 v151, v151
	v_pk_add_f32 v[164:165], v[164:165], v[144:145]
	v_pk_add_f32 v[166:167], v[166:167], v[146:147]
	v_mfma_f32_32x32x16_f16 v[96:111], v[76:79], v[12:15], v[96:111]
	v_exp_f32_e32 v152, v152
	v_exp_f32_e32 v153, v153
	v_exp_f32_e32 v154, v154
	v_exp_f32_e32 v155, v155
	v_pk_add_f32 v[164:165], v[164:165], v[148:149]
	v_pk_add_f32 v[166:167], v[166:167], v[150:151]
	v_mfma_f32_32x32x16_f16 v[112:127], v[76:79], v[28:31], v[112:127]
	v_exp_f32_e32 v156, v156
	v_exp_f32_e32 v157, v157
	v_exp_f32_e32 v158, v158
	v_exp_f32_e32 v159, v159
	v_pk_add_f32 v[164:165], v[164:165], v[152:153]
	v_pk_add_f32 v[166:167], v[166:167], v[154:155]
	s_nop 0
	v_pk_add_f32 v[164:165], v[164:165], v[156:157]
	v_pk_add_f32 v[166:167], v[166:167], v[158:159]
	global_load_dwordx4 v[64:67], v171, s[4:5] offset:0
	global_load_dwordx4 v[68:71], v171, s[4:5] offset:1024
	global_load_dwordx4 v[72:75], v171, s[4:5] offset:2048
	global_load_dwordx4 v[76:79], v171, s[4:5] offset:3072
	s_add_u32 s4, s4, 0x1000
	s_addc_u32 s5, s5, 0
	s_waitcnt vmcnt(12)
	v_mfma_f32_32x32x16_f16 v[128:143], v[80:83], v[0:3], 0
	v_exp_f32_e32 v96, v96
	v_exp_f32_e32 v97, v97
	v_exp_f32_e32 v98, v98
	v_exp_f32_e32 v99, v99
	v_mfma_f32_32x32x16_f16 v[144:159], v[80:83], v[16:19], 0
	v_exp_f32_e32 v100, v100
	v_exp_f32_e32 v101, v101
	v_exp_f32_e32 v102, v102
	v_exp_f32_e32 v103, v103
	v_pk_add_f32 v[160:161], v[160:161], v[96:97]
	v_pk_add_f32 v[162:163], v[162:163], v[98:99]
	v_mfma_f32_32x32x16_f16 v[128:143], v[84:87], v[4:7], v[128:143]
	v_exp_f32_e32 v104, v104
	v_exp_f32_e32 v105, v105
	v_exp_f32_e32 v106, v106
	v_exp_f32_e32 v107, v107
	v_pk_add_f32 v[160:161], v[160:161], v[100:101]
	v_pk_add_f32 v[162:163], v[162:163], v[102:103]
	v_mfma_f32_32x32x16_f16 v[144:159], v[84:87], v[20:23], v[144:159]
	v_exp_f32_e32 v108, v108
	v_exp_f32_e32 v109, v109
	v_exp_f32_e32 v110, v110
	v_exp_f32_e32 v111, v111
	v_pk_add_f32 v[160:161], v[160:161], v[104:105]
	v_pk_add_f32 v[162:163], v[162:163], v[106:107]
	v_mfma_f32_32x32x16_f16 v[128:143], v[88:91], v[8:11], v[128:143]
	v_exp_f32_e32 v112, v112
	v_exp_f32_e32 v113, v113
	v_exp_f32_e32 v114, v114
	v_exp_f32_e32 v115, v115
	v_pk_add_f32 v[160:161], v[160:161], v[108:109]
	v_pk_add_f32 v[162:163], v[162:163], v[110:111]
	v_mfma_f32_32x32x16_f16 v[144:159], v[88:91], v[24:27], v[144:159]
	v_exp_f32_e32 v116, v116
	v_exp_f32_e32 v117, v117
	v_exp_f32_e32 v118, v118
	v_exp_f32_e32 v119, v119
	v_pk_add_f32 v[164:165], v[164:165], v[112:113]
	v_pk_add_f32 v[166:167], v[166:167], v[114:115]
	v_mfma_f32_32x32x16_f16 v[128:143], v[92:95], v[12:15], v[128:143]
	v_exp_f32_e32 v120, v120
	v_exp_f32_e32 v121, v121
	v_exp_f32_e32 v122, v122
	v_exp_f32_e32 v123, v123
	v_pk_add_f32 v[164:165], v[164:165], v[116:117]
	v_pk_add_f32 v[166:167], v[166:167], v[118:119]
	v_mfma_f32_32x32x16_f16 v[144:159], v[92:95], v[28:31], v[144:159]
	v_exp_f32_e32 v124, v124
	v_exp_f32_e32 v125, v125
	v_exp_f32_e32 v126, v126
	v_exp_f32_e32 v127, v127
	v_pk_add_f32 v[164:165], v[164:165], v[120:121]
	v_pk_add_f32 v[166:167], v[166:167], v[122:123]
	s_nop 0
	v_pk_add_f32 v[164:165], v[164:165], v[124:125]
	v_pk_add_f32 v[166:167], v[166:167], v[126:127]
	global_load_dwordx4 v[80:83], v171, s[4:5] offset:0
	global_load_dwordx4 v[84:87], v171, s[4:5] offset:1024
	global_load_dwordx4 v[88:91], v171, s[4:5] offset:2048
	global_load_dwordx4 v[92:95], v171, s[4:5] offset:3072
	s_add_u32 s4, s4, 0x1000
	s_addc_u32 s5, s5, 0
	s_waitcnt vmcnt(12)
	v_mfma_f32_32x32x16_f16 v[96:111], v[32:35], v[0:3], 0
	v_exp_f32_e32 v128, v128
	v_exp_f32_e32 v129, v129
	v_exp_f32_e32 v130, v130
	v_exp_f32_e32 v131, v131
	v_mfma_f32_32x32x16_f16 v[112:127], v[32:35], v[16:19], 0
	v_exp_f32_e32 v132, v132
	v_exp_f32_e32 v133, v133
	v_exp_f32_e32 v134, v134
	v_exp_f32_e32 v135, v135
	v_pk_add_f32 v[160:161], v[160:161], v[128:129]
	v_pk_add_f32 v[162:163], v[162:163], v[130:131]
	v_mfma_f32_32x32x16_f16 v[96:111], v[36:39], v[4:7], v[96:111]
	v_exp_f32_e32 v136, v136
	v_exp_f32_e32 v137, v137
	v_exp_f32_e32 v138, v138
	v_exp_f32_e32 v139, v139
	v_pk_add_f32 v[160:161], v[160:161], v[132:133]
	v_pk_add_f32 v[162:163], v[162:163], v[134:135]
	v_mfma_f32_32x32x16_f16 v[112:127], v[36:39], v[20:23], v[112:127]
	v_exp_f32_e32 v140, v140
	v_exp_f32_e32 v141, v141
	v_exp_f32_e32 v142, v142
	v_exp_f32_e32 v143, v143
	v_pk_add_f32 v[160:161], v[160:161], v[136:137]
	v_pk_add_f32 v[162:163], v[162:163], v[138:139]
	v_mfma_f32_32x32x16_f16 v[96:111], v[40:43], v[8:11], v[96:111]
	v_exp_f32_e32 v144, v144
	v_exp_f32_e32 v145, v145
	v_exp_f32_e32 v146, v146
	v_exp_f32_e32 v147, v147
	v_pk_add_f32 v[160:161], v[160:161], v[140:141]
	v_pk_add_f32 v[162:163], v[162:163], v[142:143]
	v_mfma_f32_32x32x16_f16 v[112:127], v[40:43], v[24:27], v[112:127]
	v_exp_f32_e32 v148, v148
	v_exp_f32_e32 v149, v149
	v_exp_f32_e32 v150, v150
	v_exp_f32_e32 v151, v151
	v_pk_add_f32 v[164:165], v[164:165], v[144:145]
	v_pk_add_f32 v[166:167], v[166:167], v[146:147]
	v_mfma_f32_32x32x16_f16 v[96:111], v[44:47], v[12:15], v[96:111]
	v_exp_f32_e32 v152, v152
	v_exp_f32_e32 v153, v153
	v_exp_f32_e32 v154, v154
	v_exp_f32_e32 v155, v155
	v_pk_add_f32 v[164:165], v[164:165], v[148:149]
	v_pk_add_f32 v[166:167], v[166:167], v[150:151]
	v_mfma_f32_32x32x16_f16 v[112:127], v[44:47], v[28:31], v[112:127]
	v_exp_f32_e32 v156, v156
	v_exp_f32_e32 v157, v157
	v_exp_f32_e32 v158, v158
	v_exp_f32_e32 v159, v159
	v_pk_add_f32 v[164:165], v[164:165], v[152:153]
	v_pk_add_f32 v[166:167], v[166:167], v[154:155]
	s_nop 0
	v_pk_add_f32 v[164:165], v[164:165], v[156:157]
	v_pk_add_f32 v[166:167], v[166:167], v[158:159]
	global_load_dwordx4 v[32:35], v171, s[4:5] offset:0
	global_load_dwordx4 v[36:39], v171, s[4:5] offset:1024
	global_load_dwordx4 v[40:43], v171, s[4:5] offset:2048
	global_load_dwordx4 v[44:47], v171, s[4:5] offset:3072
	s_add_u32 s4, s4, 0x1000
	s_addc_u32 s5, s5, 0
	s_waitcnt vmcnt(12)
	v_mfma_f32_32x32x16_f16 v[128:143], v[48:51], v[0:3], 0
	v_exp_f32_e32 v96, v96
	v_exp_f32_e32 v97, v97
	v_exp_f32_e32 v98, v98
	v_exp_f32_e32 v99, v99
	v_mfma_f32_32x32x16_f16 v[144:159], v[48:51], v[16:19], 0
	v_exp_f32_e32 v100, v100
	v_exp_f32_e32 v101, v101
	v_exp_f32_e32 v102, v102
	v_exp_f32_e32 v103, v103
	v_pk_add_f32 v[160:161], v[160:161], v[96:97]
	v_pk_add_f32 v[162:163], v[162:163], v[98:99]
	v_mfma_f32_32x32x16_f16 v[128:143], v[52:55], v[4:7], v[128:143]
	v_exp_f32_e32 v104, v104
	v_exp_f32_e32 v105, v105
	v_exp_f32_e32 v106, v106
	v_exp_f32_e32 v107, v107
	v_pk_add_f32 v[160:161], v[160:161], v[100:101]
	v_pk_add_f32 v[162:163], v[162:163], v[102:103]
	v_mfma_f32_32x32x16_f16 v[144:159], v[52:55], v[20:23], v[144:159]
	v_exp_f32_e32 v108, v108
	v_exp_f32_e32 v109, v109
	v_exp_f32_e32 v110, v110
	v_exp_f32_e32 v111, v111
	v_pk_add_f32 v[160:161], v[160:161], v[104:105]
	v_pk_add_f32 v[162:163], v[162:163], v[106:107]
	v_mfma_f32_32x32x16_f16 v[128:143], v[56:59], v[8:11], v[128:143]
	v_exp_f32_e32 v112, v112
	v_exp_f32_e32 v113, v113
	v_exp_f32_e32 v114, v114
	v_exp_f32_e32 v115, v115
	v_pk_add_f32 v[160:161], v[160:161], v[108:109]
	v_pk_add_f32 v[162:163], v[162:163], v[110:111]
	v_mfma_f32_32x32x16_f16 v[144:159], v[56:59], v[24:27], v[144:159]
	v_exp_f32_e32 v116, v116
	v_exp_f32_e32 v117, v117
	v_exp_f32_e32 v118, v118
	v_exp_f32_e32 v119, v119
	v_pk_add_f32 v[164:165], v[164:165], v[112:113]
	v_pk_add_f32 v[166:167], v[166:167], v[114:115]
	v_mfma_f32_32x32x16_f16 v[128:143], v[60:63], v[12:15], v[128:143]
	v_exp_f32_e32 v120, v120
	v_exp_f32_e32 v121, v121
	v_exp_f32_e32 v122, v122
	v_exp_f32_e32 v123, v123
	v_pk_add_f32 v[164:165], v[164:165], v[116:117]
	v_pk_add_f32 v[166:167], v[166:167], v[118:119]
	v_mfma_f32_32x32x16_f16 v[144:159], v[60:63], v[28:31], v[144:159]
	v_exp_f32_e32 v124, v124
	v_exp_f32_e32 v125, v125
	v_exp_f32_e32 v126, v126
	v_exp_f32_e32 v127, v127
	v_pk_add_f32 v[164:165], v[164:165], v[120:121]
	v_pk_add_f32 v[166:167], v[166:167], v[122:123]
	s_nop 0
	v_pk_add_f32 v[164:165], v[164:165], v[124:125]
	v_pk_add_f32 v[166:167], v[166:167], v[126:127]
	global_load_dwordx4 v[48:51], v171, s[4:5] offset:0
	global_load_dwordx4 v[52:55], v171, s[4:5] offset:1024
	global_load_dwordx4 v[56:59], v171, s[4:5] offset:2048
	global_load_dwordx4 v[60:63], v171, s[4:5] offset:3072
	s_add_u32 s4, s4, 0x1000
	s_addc_u32 s5, s5, 0
	s_waitcnt vmcnt(12)
	v_mfma_f32_32x32x16_f16 v[96:111], v[64:67], v[0:3], 0
	v_exp_f32_e32 v128, v128
	v_exp_f32_e32 v129, v129
	v_exp_f32_e32 v130, v130
	v_exp_f32_e32 v131, v131
	v_mfma_f32_32x32x16_f16 v[112:127], v[64:67], v[16:19], 0
	v_exp_f32_e32 v132, v132
	v_exp_f32_e32 v133, v133
	v_exp_f32_e32 v134, v134
	v_exp_f32_e32 v135, v135
	v_pk_add_f32 v[160:161], v[160:161], v[128:129]
	v_pk_add_f32 v[162:163], v[162:163], v[130:131]
	v_mfma_f32_32x32x16_f16 v[96:111], v[68:71], v[4:7], v[96:111]
	v_exp_f32_e32 v136, v136
	v_exp_f32_e32 v137, v137
	v_exp_f32_e32 v138, v138
	v_exp_f32_e32 v139, v139
	v_pk_add_f32 v[160:161], v[160:161], v[132:133]
	v_pk_add_f32 v[162:163], v[162:163], v[134:135]
	v_mfma_f32_32x32x16_f16 v[112:127], v[68:71], v[20:23], v[112:127]
	v_exp_f32_e32 v140, v140
	v_exp_f32_e32 v141, v141
	v_exp_f32_e32 v142, v142
	v_exp_f32_e32 v143, v143
	v_pk_add_f32 v[160:161], v[160:161], v[136:137]
	v_pk_add_f32 v[162:163], v[162:163], v[138:139]
	v_mfma_f32_32x32x16_f16 v[96:111], v[72:75], v[8:11], v[96:111]
	v_exp_f32_e32 v144, v144
	v_exp_f32_e32 v145, v145
	v_exp_f32_e32 v146, v146
	v_exp_f32_e32 v147, v147
	v_pk_add_f32 v[160:161], v[160:161], v[140:141]
	v_pk_add_f32 v[162:163], v[162:163], v[142:143]
	v_mfma_f32_32x32x16_f16 v[112:127], v[72:75], v[24:27], v[112:127]
	v_exp_f32_e32 v148, v148
	v_exp_f32_e32 v149, v149
	v_exp_f32_e32 v150, v150
	v_exp_f32_e32 v151, v151
	v_pk_add_f32 v[164:165], v[164:165], v[144:145]
	v_pk_add_f32 v[166:167], v[166:167], v[146:147]
	v_mfma_f32_32x32x16_f16 v[96:111], v[76:79], v[12:15], v[96:111]
	v_exp_f32_e32 v152, v152
	v_exp_f32_e32 v153, v153
	v_exp_f32_e32 v154, v154
	v_exp_f32_e32 v155, v155
	v_pk_add_f32 v[164:165], v[164:165], v[148:149]
	v_pk_add_f32 v[166:167], v[166:167], v[150:151]
	v_mfma_f32_32x32x16_f16 v[112:127], v[76:79], v[28:31], v[112:127]
	v_exp_f32_e32 v156, v156
	v_exp_f32_e32 v157, v157
	v_exp_f32_e32 v158, v158
	v_exp_f32_e32 v159, v159
	v_pk_add_f32 v[164:165], v[164:165], v[152:153]
	v_pk_add_f32 v[166:167], v[166:167], v[154:155]
	s_nop 0
	v_pk_add_f32 v[164:165], v[164:165], v[156:157]
	v_pk_add_f32 v[166:167], v[166:167], v[158:159]
	global_load_dwordx4 v[64:67], v171, s[4:5] offset:0
	global_load_dwordx4 v[68:71], v171, s[4:5] offset:1024
	global_load_dwordx4 v[72:75], v171, s[4:5] offset:2048
	global_load_dwordx4 v[76:79], v171, s[4:5] offset:3072
	s_add_u32 s4, s4, 0x1000
	s_addc_u32 s5, s5, 0
	s_waitcnt vmcnt(12)
	v_mfma_f32_32x32x16_f16 v[128:143], v[80:83], v[0:3], 0
	v_exp_f32_e32 v96, v96
	v_exp_f32_e32 v97, v97
	v_exp_f32_e32 v98, v98
	v_exp_f32_e32 v99, v99
	v_mfma_f32_32x32x16_f16 v[144:159], v[80:83], v[16:19], 0
	v_exp_f32_e32 v100, v100
	v_exp_f32_e32 v101, v101
	v_exp_f32_e32 v102, v102
	v_exp_f32_e32 v103, v103
	v_pk_add_f32 v[160:161], v[160:161], v[96:97]
	v_pk_add_f32 v[162:163], v[162:163], v[98:99]
	v_mfma_f32_32x32x16_f16 v[128:143], v[84:87], v[4:7], v[128:143]
	v_exp_f32_e32 v104, v104
	v_exp_f32_e32 v105, v105
	v_exp_f32_e32 v106, v106
	v_exp_f32_e32 v107, v107
	v_pk_add_f32 v[160:161], v[160:161], v[100:101]
	v_pk_add_f32 v[162:163], v[162:163], v[102:103]
	v_mfma_f32_32x32x16_f16 v[144:159], v[84:87], v[20:23], v[144:159]
	v_exp_f32_e32 v108, v108
	v_exp_f32_e32 v109, v109
	v_exp_f32_e32 v110, v110
	v_exp_f32_e32 v111, v111
	v_pk_add_f32 v[160:161], v[160:161], v[104:105]
	v_pk_add_f32 v[162:163], v[162:163], v[106:107]
	v_mfma_f32_32x32x16_f16 v[128:143], v[88:91], v[8:11], v[128:143]
	v_exp_f32_e32 v112, v112
	v_exp_f32_e32 v113, v113
	v_exp_f32_e32 v114, v114
	v_exp_f32_e32 v115, v115
	v_pk_add_f32 v[160:161], v[160:161], v[108:109]
	v_pk_add_f32 v[162:163], v[162:163], v[110:111]
	v_mfma_f32_32x32x16_f16 v[144:159], v[88:91], v[24:27], v[144:159]
	v_exp_f32_e32 v116, v116
	v_exp_f32_e32 v117, v117
	v_exp_f32_e32 v118, v118
	v_exp_f32_e32 v119, v119
	v_pk_add_f32 v[164:165], v[164:165], v[112:113]
	v_pk_add_f32 v[166:167], v[166:167], v[114:115]
	v_mfma_f32_32x32x16_f16 v[128:143], v[92:95], v[12:15], v[128:143]
	v_exp_f32_e32 v120, v120
	v_exp_f32_e32 v121, v121
	v_exp_f32_e32 v122, v122
	v_exp_f32_e32 v123, v123
	v_pk_add_f32 v[164:165], v[164:165], v[116:117]
	v_pk_add_f32 v[166:167], v[166:167], v[118:119]
	v_mfma_f32_32x32x16_f16 v[144:159], v[92:95], v[28:31], v[144:159]
	v_exp_f32_e32 v124, v124
	v_exp_f32_e32 v125, v125
	v_exp_f32_e32 v126, v126
	v_exp_f32_e32 v127, v127
	v_pk_add_f32 v[164:165], v[164:165], v[120:121]
	v_pk_add_f32 v[166:167], v[166:167], v[122:123]
	s_nop 0
	v_pk_add_f32 v[164:165], v[164:165], v[124:125]
	v_pk_add_f32 v[166:167], v[166:167], v[126:127]
	global_load_dwordx4 v[80:83], v171, s[4:5] offset:0
	global_load_dwordx4 v[84:87], v171, s[4:5] offset:1024
	global_load_dwordx4 v[88:91], v171, s[4:5] offset:2048
	global_load_dwordx4 v[92:95], v171, s[4:5] offset:3072
	s_add_u32 s4, s4, 0x1000
	s_addc_u32 s5, s5, 0
	s_waitcnt vmcnt(12)
	v_mfma_f32_32x32x16_f16 v[96:111], v[32:35], v[0:3], 0
	v_exp_f32_e32 v128, v128
	v_exp_f32_e32 v129, v129
	v_exp_f32_e32 v130, v130
	v_exp_f32_e32 v131, v131
	v_mfma_f32_32x32x16_f16 v[112:127], v[32:35], v[16:19], 0
	v_exp_f32_e32 v132, v132
	v_exp_f32_e32 v133, v133
	v_exp_f32_e32 v134, v134
	v_exp_f32_e32 v135, v135
	v_pk_add_f32 v[160:161], v[160:161], v[128:129]
	v_pk_add_f32 v[162:163], v[162:163], v[130:131]
	v_mfma_f32_32x32x16_f16 v[96:111], v[36:39], v[4:7], v[96:111]
	v_exp_f32_e32 v136, v136
	v_exp_f32_e32 v137, v137
	v_exp_f32_e32 v138, v138
	v_exp_f32_e32 v139, v139
	v_pk_add_f32 v[160:161], v[160:161], v[132:133]
	v_pk_add_f32 v[162:163], v[162:163], v[134:135]
	v_mfma_f32_32x32x16_f16 v[112:127], v[36:39], v[20:23], v[112:127]
	v_exp_f32_e32 v140, v140
	v_exp_f32_e32 v141, v141
	v_exp_f32_e32 v142, v142
	v_exp_f32_e32 v143, v143
	v_pk_add_f32 v[160:161], v[160:161], v[136:137]
	v_pk_add_f32 v[162:163], v[162:163], v[138:139]
	v_mfma_f32_32x32x16_f16 v[96:111], v[40:43], v[8:11], v[96:111]
	v_exp_f32_e32 v144, v144
	v_exp_f32_e32 v145, v145
	v_exp_f32_e32 v146, v146
	v_exp_f32_e32 v147, v147
	v_pk_add_f32 v[160:161], v[160:161], v[140:141]
	v_pk_add_f32 v[162:163], v[162:163], v[142:143]
	v_mfma_f32_32x32x16_f16 v[112:127], v[40:43], v[24:27], v[112:127]
	v_exp_f32_e32 v148, v148
	v_exp_f32_e32 v149, v149
	v_exp_f32_e32 v150, v150
	v_exp_f32_e32 v151, v151
	v_pk_add_f32 v[164:165], v[164:165], v[144:145]
	v_pk_add_f32 v[166:167], v[166:167], v[146:147]
	v_mfma_f32_32x32x16_f16 v[96:111], v[44:47], v[12:15], v[96:111]
	v_exp_f32_e32 v152, v152
	v_exp_f32_e32 v153, v153
	v_exp_f32_e32 v154, v154
	v_exp_f32_e32 v155, v155
	v_pk_add_f32 v[164:165], v[164:165], v[148:149]
	v_pk_add_f32 v[166:167], v[166:167], v[150:151]
	v_mfma_f32_32x32x16_f16 v[112:127], v[44:47], v[28:31], v[112:127]
	v_exp_f32_e32 v156, v156
	v_exp_f32_e32 v157, v157
	v_exp_f32_e32 v158, v158
	v_exp_f32_e32 v159, v159
	v_pk_add_f32 v[164:165], v[164:165], v[152:153]
	v_pk_add_f32 v[166:167], v[166:167], v[154:155]
	s_nop 0
	v_pk_add_f32 v[164:165], v[164:165], v[156:157]
	v_pk_add_f32 v[166:167], v[166:167], v[158:159]
	s_waitcnt vmcnt(8)
	v_mfma_f32_32x32x16_f16 v[128:143], v[48:51], v[0:3], 0
	v_exp_f32_e32 v96, v96
	v_exp_f32_e32 v97, v97
	v_exp_f32_e32 v98, v98
	v_exp_f32_e32 v99, v99
	v_mfma_f32_32x32x16_f16 v[144:159], v[48:51], v[16:19], 0
	v_exp_f32_e32 v100, v100
	v_exp_f32_e32 v101, v101
	v_exp_f32_e32 v102, v102
	v_exp_f32_e32 v103, v103
	v_pk_add_f32 v[160:161], v[160:161], v[96:97]
	v_pk_add_f32 v[162:163], v[162:163], v[98:99]
	v_mfma_f32_32x32x16_f16 v[128:143], v[52:55], v[4:7], v[128:143]
	v_exp_f32_e32 v104, v104
	v_exp_f32_e32 v105, v105
	v_exp_f32_e32 v106, v106
	v_exp_f32_e32 v107, v107
	v_pk_add_f32 v[160:161], v[160:161], v[100:101]
	v_pk_add_f32 v[162:163], v[162:163], v[102:103]
	v_mfma_f32_32x32x16_f16 v[144:159], v[52:55], v[20:23], v[144:159]
	v_exp_f32_e32 v108, v108
	v_exp_f32_e32 v109, v109
	v_exp_f32_e32 v110, v110
	v_exp_f32_e32 v111, v111
	v_pk_add_f32 v[160:161], v[160:161], v[104:105]
	v_pk_add_f32 v[162:163], v[162:163], v[106:107]
	v_mfma_f32_32x32x16_f16 v[128:143], v[56:59], v[8:11], v[128:143]
	v_exp_f32_e32 v112, v112
	v_exp_f32_e32 v113, v113
	v_exp_f32_e32 v114, v114
	v_exp_f32_e32 v115, v115
	v_pk_add_f32 v[160:161], v[160:161], v[108:109]
	v_pk_add_f32 v[162:163], v[162:163], v[110:111]
	v_mfma_f32_32x32x16_f16 v[144:159], v[56:59], v[24:27], v[144:159]
	v_exp_f32_e32 v116, v116
	v_exp_f32_e32 v117, v117
	v_exp_f32_e32 v118, v118
	v_exp_f32_e32 v119, v119
	v_pk_add_f32 v[164:165], v[164:165], v[112:113]
	v_pk_add_f32 v[166:167], v[166:167], v[114:115]
	v_mfma_f32_32x32x16_f16 v[128:143], v[60:63], v[12:15], v[128:143]
	v_exp_f32_e32 v120, v120
	v_exp_f32_e32 v121, v121
	v_exp_f32_e32 v122, v122
	v_exp_f32_e32 v123, v123
	v_pk_add_f32 v[164:165], v[164:165], v[116:117]
	v_pk_add_f32 v[166:167], v[166:167], v[118:119]
	v_mfma_f32_32x32x16_f16 v[144:159], v[60:63], v[28:31], v[144:159]
	v_exp_f32_e32 v124, v124
	v_exp_f32_e32 v125, v125
	v_exp_f32_e32 v126, v126
	v_exp_f32_e32 v127, v127
	v_pk_add_f32 v[164:165], v[164:165], v[120:121]
	v_pk_add_f32 v[166:167], v[166:167], v[122:123]
	s_nop 0
	v_pk_add_f32 v[164:165], v[164:165], v[124:125]
	v_pk_add_f32 v[166:167], v[166:167], v[126:127]
	s_waitcnt vmcnt(4)
	v_mfma_f32_32x32x16_f16 v[96:111], v[64:67], v[0:3], 0
	v_exp_f32_e32 v128, v128
	v_exp_f32_e32 v129, v129
	v_exp_f32_e32 v130, v130
	v_exp_f32_e32 v131, v131
	v_mfma_f32_32x32x16_f16 v[112:127], v[64:67], v[16:19], 0
	v_exp_f32_e32 v132, v132
	v_exp_f32_e32 v133, v133
	v_exp_f32_e32 v134, v134
	v_exp_f32_e32 v135, v135
	v_pk_add_f32 v[160:161], v[160:161], v[128:129]
	v_pk_add_f32 v[162:163], v[162:163], v[130:131]
	v_mfma_f32_32x32x16_f16 v[96:111], v[68:71], v[4:7], v[96:111]
	v_exp_f32_e32 v136, v136
	v_exp_f32_e32 v137, v137
	v_exp_f32_e32 v138, v138
	v_exp_f32_e32 v139, v139
	v_pk_add_f32 v[160:161], v[160:161], v[132:133]
	v_pk_add_f32 v[162:163], v[162:163], v[134:135]
	v_mfma_f32_32x32x16_f16 v[112:127], v[68:71], v[20:23], v[112:127]
	v_exp_f32_e32 v140, v140
	v_exp_f32_e32 v141, v141
	v_exp_f32_e32 v142, v142
	v_exp_f32_e32 v143, v143
	v_pk_add_f32 v[160:161], v[160:161], v[136:137]
	v_pk_add_f32 v[162:163], v[162:163], v[138:139]
	v_mfma_f32_32x32x16_f16 v[96:111], v[72:75], v[8:11], v[96:111]
	v_exp_f32_e32 v144, v144
	v_exp_f32_e32 v145, v145
	v_exp_f32_e32 v146, v146
	v_exp_f32_e32 v147, v147
	v_pk_add_f32 v[160:161], v[160:161], v[140:141]
	v_pk_add_f32 v[162:163], v[162:163], v[142:143]
	v_mfma_f32_32x32x16_f16 v[112:127], v[72:75], v[24:27], v[112:127]
	v_exp_f32_e32 v148, v148
	v_exp_f32_e32 v149, v149
	v_exp_f32_e32 v150, v150
	v_exp_f32_e32 v151, v151
	v_pk_add_f32 v[164:165], v[164:165], v[144:145]
	v_pk_add_f32 v[166:167], v[166:167], v[146:147]
	v_mfma_f32_32x32x16_f16 v[96:111], v[76:79], v[12:15], v[96:111]
	v_exp_f32_e32 v152, v152
	v_exp_f32_e32 v153, v153
	v_exp_f32_e32 v154, v154
	v_exp_f32_e32 v155, v155
	v_pk_add_f32 v[164:165], v[164:165], v[148:149]
	v_pk_add_f32 v[166:167], v[166:167], v[150:151]
	v_mfma_f32_32x32x16_f16 v[112:127], v[76:79], v[28:31], v[112:127]
	v_exp_f32_e32 v156, v156
	v_exp_f32_e32 v157, v157
	v_exp_f32_e32 v158, v158
	v_exp_f32_e32 v159, v159
	v_pk_add_f32 v[164:165], v[164:165], v[152:153]
	v_pk_add_f32 v[166:167], v[166:167], v[154:155]
	s_nop 0
	v_pk_add_f32 v[164:165], v[164:165], v[156:157]
	v_pk_add_f32 v[166:167], v[166:167], v[158:159]
	s_waitcnt vmcnt(0)
	v_mfma_f32_32x32x16_f16 v[128:143], v[80:83], v[0:3], 0
	v_exp_f32_e32 v96, v96
	v_exp_f32_e32 v97, v97
	v_exp_f32_e32 v98, v98
	v_exp_f32_e32 v99, v99
	v_mfma_f32_32x32x16_f16 v[144:159], v[80:83], v[16:19], 0
	v_exp_f32_e32 v100, v100
	v_exp_f32_e32 v101, v101
	v_exp_f32_e32 v102, v102
	v_exp_f32_e32 v103, v103
	v_pk_add_f32 v[160:161], v[160:161], v[96:97]
	v_pk_add_f32 v[162:163], v[162:163], v[98:99]
	v_mfma_f32_32x32x16_f16 v[128:143], v[84:87], v[4:7], v[128:143]
	v_exp_f32_e32 v104, v104
	v_exp_f32_e32 v105, v105
	v_exp_f32_e32 v106, v106
	v_exp_f32_e32 v107, v107
	v_pk_add_f32 v[160:161], v[160:161], v[100:101]
	v_pk_add_f32 v[162:163], v[162:163], v[102:103]
	v_mfma_f32_32x32x16_f16 v[144:159], v[84:87], v[20:23], v[144:159]
	v_exp_f32_e32 v108, v108
	v_exp_f32_e32 v109, v109
	v_exp_f32_e32 v110, v110
	v_exp_f32_e32 v111, v111
	v_pk_add_f32 v[160:161], v[160:161], v[104:105]
	v_pk_add_f32 v[162:163], v[162:163], v[106:107]
	v_mfma_f32_32x32x16_f16 v[128:143], v[88:91], v[8:11], v[128:143]
	v_exp_f32_e32 v112, v112
	v_exp_f32_e32 v113, v113
	v_exp_f32_e32 v114, v114
	v_exp_f32_e32 v115, v115
	v_pk_add_f32 v[160:161], v[160:161], v[108:109]
	v_pk_add_f32 v[162:163], v[162:163], v[110:111]
	v_mfma_f32_32x32x16_f16 v[144:159], v[88:91], v[24:27], v[144:159]
	v_exp_f32_e32 v116, v116
	v_exp_f32_e32 v117, v117
	v_exp_f32_e32 v118, v118
	v_exp_f32_e32 v119, v119
	v_pk_add_f32 v[164:165], v[164:165], v[112:113]
	v_pk_add_f32 v[166:167], v[166:167], v[114:115]
	v_mfma_f32_32x32x16_f16 v[128:143], v[92:95], v[12:15], v[128:143]
	v_exp_f32_e32 v120, v120
	v_exp_f32_e32 v121, v121
	v_exp_f32_e32 v122, v122
	v_exp_f32_e32 v123, v123
	v_pk_add_f32 v[164:165], v[164:165], v[116:117]
	v_pk_add_f32 v[166:167], v[166:167], v[118:119]
	v_mfma_f32_32x32x16_f16 v[144:159], v[92:95], v[28:31], v[144:159]
	v_exp_f32_e32 v124, v124
	v_exp_f32_e32 v125, v125
	v_exp_f32_e32 v126, v126
	v_exp_f32_e32 v127, v127
	v_pk_add_f32 v[164:165], v[164:165], v[120:121]
	v_pk_add_f32 v[166:167], v[166:167], v[122:123]
	s_nop 0
	v_pk_add_f32 v[164:165], v[164:165], v[124:125]
	v_pk_add_f32 v[166:167], v[166:167], v[126:127]
	v_exp_f32_e32 v128, v128
	v_exp_f32_e32 v129, v129
	v_exp_f32_e32 v130, v130
	v_exp_f32_e32 v131, v131
	v_exp_f32_e32 v132, v132
	v_exp_f32_e32 v133, v133
	v_exp_f32_e32 v134, v134
	v_exp_f32_e32 v135, v135
	v_pk_add_f32 v[160:161], v[160:161], v[128:129]
	v_pk_add_f32 v[162:163], v[162:163], v[130:131]
	v_exp_f32_e32 v136, v136
	v_exp_f32_e32 v137, v137
	v_exp_f32_e32 v138, v138
	v_exp_f32_e32 v139, v139
	v_pk_add_f32 v[160:161], v[160:161], v[132:133]
	v_pk_add_f32 v[162:163], v[162:163], v[134:135]
	v_exp_f32_e32 v140, v140
	v_exp_f32_e32 v141, v141
	v_exp_f32_e32 v142, v142
	v_exp_f32_e32 v143, v143
	v_pk_add_f32 v[160:161], v[160:161], v[136:137]
	v_pk_add_f32 v[162:163], v[162:163], v[138:139]
	v_exp_f32_e32 v144, v144
	v_exp_f32_e32 v145, v145
	v_exp_f32_e32 v146, v146
	v_exp_f32_e32 v147, v147
	v_pk_add_f32 v[160:161], v[160:161], v[140:141]
	v_pk_add_f32 v[162:163], v[162:163], v[142:143]
	v_exp_f32_e32 v148, v148
	v_exp_f32_e32 v149, v149
	v_exp_f32_e32 v150, v150
	v_exp_f32_e32 v151, v151
	v_pk_add_f32 v[164:165], v[164:165], v[144:145]
	v_pk_add_f32 v[166:167], v[166:167], v[146:147]
	v_exp_f32_e32 v152, v152
	v_exp_f32_e32 v153, v153
	v_exp_f32_e32 v154, v154
	v_exp_f32_e32 v155, v155
	v_pk_add_f32 v[164:165], v[164:165], v[148:149]
	v_pk_add_f32 v[166:167], v[166:167], v[150:151]
	v_exp_f32_e32 v156, v156
	v_exp_f32_e32 v157, v157
	v_exp_f32_e32 v158, v158
	v_exp_f32_e32 v159, v159
	v_pk_add_f32 v[164:165], v[164:165], v[152:153]
	v_pk_add_f32 v[166:167], v[166:167], v[154:155]
	s_nop 0
	v_pk_add_f32 v[164:165], v[164:165], v[156:157]
	v_pk_add_f32 v[166:167], v[166:167], v[158:159]
	v_add_f32_e32 v160, v160, v161
	v_add_f32_e32 v162, v162, v163
	v_add_f32_e32 v164, v164, v165
	v_add_f32_e32 v166, v166, v167
	v_add_f32_e32 v160, v160, v162
	v_add_f32_e32 v164, v164, v166
	v_lshrrev_b32_e32 v168, 5, v172
	v_and_b32_e32 v169, 31, v172
	v_lshlrev_b32_e32 v168, 8, v168
	v_lshl_add_u32 v168, v173, 9, v168
	v_lshl_add_u32 v168, v169, 2, v168
	ds_write2_b32 v168, v160, v164 offset1:32
	s_waitcnt lgkmcnt(0)
	s_barrier
	s_cmp_lg_u32 s14, 0
	s_cbranch_scc1 .Lk2_done
	v_lshlrev_b32_e32 v168, 2, v170
	ds_read_b32 v0, v168 offset:0
	ds_read_b32 v1, v168 offset:256
	ds_read_b32 v2, v168 offset:512
	ds_read_b32 v3, v168 offset:768
	ds_read_b32 v4, v168 offset:1024
	ds_read_b32 v5, v168 offset:1280
	ds_read_b32 v6, v168 offset:1536
	ds_read_b32 v7, v168 offset:1792
	ds_read_b32 v8, v168 offset:2048
	ds_read_b32 v9, v168 offset:2304
	ds_read_b32 v10, v168 offset:2560
	ds_read_b32 v11, v168 offset:2816
	ds_read_b32 v12, v168 offset:3072
	ds_read_b32 v13, v168 offset:3328
	ds_read_b32 v14, v168 offset:3584
	ds_read_b32 v15, v168 offset:3840
	s_waitcnt lgkmcnt(0)
	v_add_f32_e32 v0, v0, v1
	v_add_f32_e32 v0, v0, v2
	v_add_f32_e32 v0, v0, v3
	v_add_f32_e32 v0, v0, v4
	v_add_f32_e32 v0, v0, v5
	v_add_f32_e32 v0, v0, v6
	v_add_f32_e32 v0, v0, v7
	v_add_f32_e32 v0, v0, v8
	v_add_f32_e32 v0, v0, v9
	v_add_f32_e32 v0, v0, v10
	v_add_f32_e32 v0, v0, v11
	v_add_f32_e32 v0, v0, v12
	v_add_f32_e32 v0, v0, v13
	v_add_f32_e32 v0, v0, v14
	v_add_f32_e32 v0, v0, v15
	v_log_f32_e32 v0, v0
	s_lshl_b32 s10, s10, 12
	s_lshl_b32 s11, s11, 5
	s_add_u32 s10, s10, s11
	v_add_u32_e32 v1, s10, v170
	v_lshlrev_b32_e32 v1, 2, v1
	v_sub_f32_e32 v0, 0x41400000, v0
	global_store_dword v1, v0, s[8:9] sc1
